# out-projection GEMM epilogue: the 32 residual loads issued in two batches of 16 ahead of the adds and stores instead of load, wait, add, store one piece at a time
# speedup vs baseline: 1.0086x; 1.0076x over previous
; template <class Epi, class Sched, bool FP8 = false>
; __device__ __forceinline__ void gemm_phase(LAS unsigned char* lds, const int Kb, const int nt  , const Sched& S, const Epi& E) {
;     ...
;         if (!has_next) break;
; #pragma unroll
;         for (int a = 0; a < 2; ++a)
; #pragma unroll
;             for (int b = 0; b < 2; ++b)
; #pragma unroll
;                 for (int m = 0; m < 4; ++m)
; #pragma unroll
;                     for (int n = 0; n < 2; ++n) acc[a][b][m][n] = (f32x4){0.f, 0.f, 0.f, 0.f};
;         cur = nxt; cA = nA; cB = nB; ++ui;
.Lepi_done_1715:
	s_and_b64 vcc, exec, s[14:15]
	s_mov_b32 s56, s55
	s_mov_b32 s2, s16
	s_mov_b64 s[24:25], s[20:21]
	s_mov_b64 s[22:23], s[18:19]
	s_cbranch_vccnz .LBB0_1780

; #define PG8_STAGE(bufoff, gbase, voff) do { _Pragma("unroll") for (int _i = 0; _i < 2; ++_i) glds16_s((const void*)((const char*)(gbase) + _i * r64), (voff), ldsb + (unsigned)(bufoff) + ldsw + _i * 8192u); } while (0)
; #define PG8_LDA(b, h) do { _Pragma("unroll") for (int m = 0; m < 4; ++m) { const int o_ = PG8_SA(b, h) + aoff + m * 2048; \
;         if constexpr (FP8) A8[m] = PG8_CAT8(o_); else { At[m][0] = PG8_LD16(o_); At[m][1] = PG8_LD16(o_ + 1024); } } } while (0)
; #define PG8_LDB(X, X8, b, h) do { _Pragma("unroll") for (int n = 0; n < 2; ++n) { const int o_ = PG8_SB(b, h) + boff + n * 2048; \
;         if constexpr (FP8) X8[n] = PG8_CAT8(o_); else { X[n][0] = PG8_LD16(o_); X[n][1] = PG8_LD16(o_ + 1024); } } } while (0)
; #define PG8_WAIT_V(n) asm volatile("s_waitcnt vmcnt(" #n ")" ::: "memory")
; #define PG8_WAIT_L(n) asm volatile("s_waitcnt lgkmcnt(" #n ")" ::: "memory")
; #define PG8_BAR __builtin_amdgcn_s_barrier()
; #define PG8_SCHED __builtin_amdgcn_sched_barrier(0)
; #define PG8_HI do { if constexpr (FP8) asm volatile("s_setprio 1"); } while (0)
; #define PG8_LO do { if constexpr (FP8) asm volatile("s_setprio 0"); } while (0)
; template <class Epi, class Sched, bool FP8 = false>
; __device__ __forceinline__ void gemm_phase(LAS unsigned char* lds, const int Kb, const int nt  , const Sched& S, const Epi& E) {
;     ...
;             PG8_LDB(B0, B08, 0, 0); PG8_SCHED; PG8_LDA(0, 0); PG8_STAGE(PG8_SA(1, 1), a1 + hstep, voffA);
;             PG8_WAIT_L(8); PG8_BAR; PG8_HI; PG8_WAIT_L(0); PG8_MMA(0, 0, B0, B08); PG8_BAR; PG8_LO; PG8_SCHED;
;             PG8_LDB(B1, B18, 0, 1); PG8_STAGE(PG8_SB(0, 0), b2, voffB);
;             PG8_BAR; PG8_HI; PG8_WAIT_L(0); PG8_MMA(0, 1, B1, B18); PG8_BAR; PG8_LO;
;             PG8_LDA(0, 1); PG8_STAGE(PG8_SA(0, 0), a2, voffA);
;             PG8_BAR; PG8_HI; PG8_WAIT_L(0); PG8_MMA(1, 0, B0, B08); PG8_BAR; PG8_LO; PG8_SCHED;
;             PG8_STAGE(PG8_SB(0, 1), b2 + hstep, voffB);
;             PG8_WAIT_V(6); PG8_BAR; PG8_HI; PG8_MMA(1, 1, B1, B18); PG8_BAR; PG8_LO;
.LBB0_1715:
	ds_read_b128 v[130:133], v138
	ds_read_b128 v[134:137], v139
	ds_read_b128 v[156:159], v140
	ds_read_b128 v[160:163], v141
	s_add_u32 s24, s22, 0xfff80080
	s_addc_u32 s25, s23, -1
	s_cmp_eq_u32 s57, 28
	s_cselect_b32 s26, s18, s24
	s_cselect_b32 s27, s19, s25
	s_cselect_b32 s24, s20, s3
	s_cselect_b32 s25, s21, s17
	s_add_u32 s28, s26, 0x80
	s_addc_u32 s29, s27, 0
	ds_read_b128 v[164:167], v154
	ds_read_b128 v[168:171], v154 offset:1024
	ds_read_b128 v[172:175], v154 offset:2048
	ds_read_b128 v[176:179], v154 offset:3072
	ds_read_b128 v[180:183], v154 offset:4096
	ds_read_b128 v[184:187], v154 offset:5120
	ds_read_b128 v[194:197], v154 offset:6144
	ds_read_b128 v[198:201], v154 offset:7168
	s_mov_b32 s58, m0
	s_mov_b32 m0, s53
	s_nop 0
	global_load_lds_dwordx4 v1, s[22:23]
	s_mov_b32 m0, s58
	s_add_u32 s58, s22, 0x40000
	s_addc_u32 s59, s23, 0
	s_mov_b32 s60, m0
	s_mov_b32 m0, s54
	s_nop 0
	global_load_lds_dwordx4 v1, s[58:59]
	s_mov_b32 m0, s60
	s_waitcnt lgkmcnt(8)
	s_barrier
	s_waitcnt lgkmcnt(0)
	s_setprio 1
	v_mfma_f32_16x16x32_bf16 v[126:129], v[130:133], v[164:167], v[126:129]
	v_mfma_f32_16x16x32_bf16 v[122:125], v[156:159], v[164:167], v[122:125]
	v_mfma_f32_16x16x32_bf16 v[110:113], v[130:133], v[172:175], v[110:113]
	v_mfma_f32_16x16x32_bf16 v[106:109], v[156:159], v[172:175], v[106:109]
	v_mfma_f32_16x16x32_bf16 v[94:97], v[130:133], v[180:183], v[94:97]
	v_mfma_f32_16x16x32_bf16 v[90:93], v[156:159], v[180:183], v[90:93]
	v_mfma_f32_16x16x32_bf16 v[78:81], v[130:133], v[194:197], v[78:81]
	v_mfma_f32_16x16x32_bf16 v[74:77], v[156:159], v[194:197], v[74:77]
	v_mfma_f32_16x16x32_bf16 v[126:129], v[134:137], v[168:171], v[126:129]
	v_mfma_f32_16x16x32_bf16 v[122:125], v[160:163], v[168:171], v[122:125]
	v_mfma_f32_16x16x32_bf16 v[110:113], v[134:137], v[176:179], v[110:113]
	v_mfma_f32_16x16x32_bf16 v[106:109], v[160:163], v[176:179], v[106:109]
	v_mfma_f32_16x16x32_bf16 v[94:97], v[134:137], v[184:187], v[94:97]
	v_mfma_f32_16x16x32_bf16 v[90:93], v[160:163], v[184:187], v[90:93]
	v_mfma_f32_16x16x32_bf16 v[78:81], v[134:137], v[198:201], v[78:81]
	v_mfma_f32_16x16x32_bf16 v[74:77], v[160:163], v[198:201], v[74:77]
	s_setprio 0
	s_barrier
	ds_read_b128 v[202:205], v142
	ds_read_b128 v[206:209], v143
	ds_read_b128 v[210:213], v144
	ds_read_b128 v[214:217], v145
	s_mov_b32 s58, m0
	s_mov_b32 m0, s38
	s_nop 0
	global_load_lds_dwordx4 v1, s[24:25]
	s_mov_b32 m0, s58
	s_add_u32 s58, s24, 0x40000
	s_addc_u32 s59, s25, 0
	s_mov_b32 s60, m0
	s_mov_b32 m0, s39
	s_nop 0
	global_load_lds_dwordx4 v1, s[58:59]
	s_mov_b32 m0, s60
	s_barrier
	s_waitcnt lgkmcnt(0)
	s_setprio 1
	v_mfma_f32_16x16x32_bf16 v[118:121], v[202:205], v[164:167], v[118:121]
	v_mfma_f32_16x16x32_bf16 v[114:117], v[210:213], v[164:167], v[114:117]
	v_mfma_f32_16x16x32_bf16 v[102:105], v[202:205], v[172:175], v[102:105]
	v_mfma_f32_16x16x32_bf16 v[98:101], v[210:213], v[172:175], v[98:101]
	v_mfma_f32_16x16x32_bf16 v[86:89], v[202:205], v[180:183], v[86:89]
	v_mfma_f32_16x16x32_bf16 v[82:85], v[210:213], v[180:183], v[82:85]
	v_mfma_f32_16x16x32_bf16 v[70:73], v[202:205], v[194:197], v[70:73]
	v_mfma_f32_16x16x32_bf16 v[66:69], v[210:213], v[194:197], v[66:69]
	v_mfma_f32_16x16x32_bf16 v[118:121], v[206:209], v[168:171], v[118:121]
	v_mfma_f32_16x16x32_bf16 v[114:117], v[214:217], v[168:171], v[114:117]
	v_mfma_f32_16x16x32_bf16 v[102:105], v[206:209], v[176:179], v[102:105]
	v_mfma_f32_16x16x32_bf16 v[98:101], v[214:217], v[176:179], v[98:101]
	v_mfma_f32_16x16x32_bf16 v[86:89], v[206:209], v[184:187], v[86:89]
	v_mfma_f32_16x16x32_bf16 v[82:85], v[214:217], v[184:187], v[82:85]
	v_mfma_f32_16x16x32_bf16 v[70:73], v[206:209], v[198:201], v[70:73]
	v_mfma_f32_16x16x32_bf16 v[66:69], v[214:217], v[198:201], v[66:69]
	s_setprio 0
	s_barrier
	ds_read_b128 v[164:167], v154 offset:16384
	ds_read_b128 v[168:171], v154 offset:17408
	ds_read_b128 v[172:175], v154 offset:18432
	ds_read_b128 v[176:179], v154 offset:19456
	ds_read_b128 v[180:183], v154 offset:20480
	ds_read_b128 v[184:187], v154 offset:21504
	ds_read_b128 v[194:197], v154 offset:22528
	ds_read_b128 v[198:201], v154 offset:23552
	s_mov_b32 s58, m0
	s_mov_b32 m0, s37
	s_nop 0
	global_load_lds_dwordx4 v1, s[26:27]
	s_mov_b32 m0, s58
	s_add_u32 s58, s26, 0x40000
	s_addc_u32 s59, s27, 0
	s_mov_b32 s60, m0
	s_mov_b32 m0, s40
	s_nop 0
	global_load_lds_dwordx4 v1, s[58:59]
	s_mov_b32 m0, s60
	s_barrier
	s_waitcnt lgkmcnt(0)
	s_setprio 1
	v_mfma_f32_16x16x32_bf16 v[62:65], v[130:133], v[164:167], v[62:65]
	v_mfma_f32_16x16x32_bf16 v[58:61], v[156:159], v[164:167], v[58:61]
	v_mfma_f32_16x16x32_bf16 v[46:49], v[130:133], v[172:175], v[46:49]
	v_mfma_f32_16x16x32_bf16 v[42:45], v[156:159], v[172:175], v[42:45]
	v_mfma_f32_16x16x32_bf16 v[30:33], v[130:133], v[180:183], v[30:33]
	v_mfma_f32_16x16x32_bf16 v[26:29], v[156:159], v[180:183], v[26:29]
	v_mfma_f32_16x16x32_bf16 v[14:17], v[130:133], v[194:197], v[14:17]
	v_mfma_f32_16x16x32_bf16 v[10:13], v[156:159], v[194:197], v[10:13]
	v_mfma_f32_16x16x32_bf16 v[62:65], v[134:137], v[168:171], v[62:65]
	v_mfma_f32_16x16x32_bf16 v[58:61], v[160:163], v[168:171], v[58:61]
	v_mfma_f32_16x16x32_bf16 v[46:49], v[134:137], v[176:179], v[46:49]
	v_mfma_f32_16x16x32_bf16 v[42:45], v[160:163], v[176:179], v[42:45]
	v_mfma_f32_16x16x32_bf16 v[30:33], v[134:137], v[184:187], v[30:33]
	v_mfma_f32_16x16x32_bf16 v[26:29], v[160:163], v[184:187], v[26:29]
	v_mfma_f32_16x16x32_bf16 v[14:17], v[134:137], v[198:201], v[14:17]
	v_mfma_f32_16x16x32_bf16 v[10:13], v[160:163], v[198:201], v[10:13]
	s_setprio 0
	s_barrier
; #define PG8_STAGE(bufoff, gbase, voff) do { _Pragma("unroll") for (int _i = 0; _i < 2; ++_i) glds16_s((const void*)((const char*)(gbase) + _i * r64), (voff), ldsb + (unsigned)(bufoff) + ldsw + _i * 8192u); } while (0)
; #define PG8_LDA(b, h) do { _Pragma("unroll") for (int m = 0; m < 4; ++m) { const int o_ = PG8_SA(b, h) + aoff + m * 2048; \
;         if constexpr (FP8) A8[m] = PG8_CAT8(o_); else { At[m][0] = PG8_LD16(o_); At[m][1] = PG8_LD16(o_ + 1024); } } } while (0)
; #define PG8_LDB(X, X8, b, h) do { _Pragma("unroll") for (int n = 0; n < 2; ++n) { const int o_ = PG8_SB(b, h) + boff + n * 2048; \
;         if constexpr (FP8) X8[n] = PG8_CAT8(o_); else { X[n][0] = PG8_LD16(o_); X[n][1] = PG8_LD16(o_ + 1024); } } } while (0)
; #define PG8_WAIT_V(n) asm volatile("s_waitcnt vmcnt(" #n ")" ::: "memory")
; #define PG8_WAIT_L(n) asm volatile("s_waitcnt lgkmcnt(" #n ")" ::: "memory")
; #define PG8_BAR __builtin_amdgcn_s_barrier()
; #define PG8_SCHED __builtin_amdgcn_sched_barrier(0)
; #define PG8_HI do { if constexpr (FP8) asm volatile("s_setprio 1"); } while (0)
; #define PG8_LO do { if constexpr (FP8) asm volatile("s_setprio 0"); } while (0)
; template <class Epi, class Sched, bool FP8 = false>
; __device__ __forceinline__ void gemm_phase(LAS unsigned char* lds, const int Kb, const int nt  , const Sched& S, const Epi& E) {
;     ...
;             PG8_WAIT_V(6); PG8_BAR; PG8_HI; PG8_MMA(1, 1, B1, B18); PG8_BAR; PG8_LO;
;             PG8_LDB(B0, B08, 1, 0); PG8_SCHED; PG8_LDA(1, 0); PG8_STAGE(PG8_SA(0, 1), a2 + hstep, voffA);
;             PG8_WAIT_L(8); PG8_BAR; PG8_HI; PG8_WAIT_L(0); PG8_MMA(0, 0, B0, B08); PG8_BAR; PG8_LO; PG8_SCHED;
;             PG8_LDB(B1, B18, 1, 1); PG8_STAGE(PG8_SB(1, 0), b3, voffB);
;             PG8_BAR; PG8_HI; PG8_WAIT_L(0); PG8_MMA(0, 1, B1, B18); PG8_BAR; PG8_LO;
;             PG8_LDA(1, 1); PG8_STAGE(PG8_SA(1, 0), a3, voffA);
;             PG8_BAR; PG8_HI; PG8_WAIT_L(0); PG8_MMA(1, 0, B0, B08); PG8_BAR; PG8_LO; PG8_SCHED;
	s_add_u32 s58, s24, 0x80000
	s_addc_u32 s59, s25, 0
	s_mov_b32 s60, m0
	s_mov_b32 m0, s41
	s_nop 0
	global_load_lds_dwordx4 v1, s[58:59]
	s_mov_b32 m0, s60
	s_add_u32 s58, s24, 0xc0000
	s_addc_u32 s59, s25, 0
	s_mov_b32 s60, m0
	s_mov_b32 m0, s42
	s_nop 0
	global_load_lds_dwordx4 v1, s[58:59]
	s_mov_b32 m0, s60
	s_waitcnt vmcnt(6)
	s_barrier
	s_setprio 1
	v_mfma_f32_16x16x32_bf16 v[54:57], v[202:205], v[164:167], v[54:57]
	v_mfma_f32_16x16x32_bf16 v[50:53], v[210:213], v[164:167], v[50:53]
	v_mfma_f32_16x16x32_bf16 v[38:41], v[202:205], v[172:175], v[38:41]
	v_mfma_f32_16x16x32_bf16 v[34:37], v[210:213], v[172:175], v[34:37]
	v_mfma_f32_16x16x32_bf16 v[22:25], v[202:205], v[180:183], v[22:25]
	v_mfma_f32_16x16x32_bf16 v[18:21], v[210:213], v[180:183], v[18:21]
	v_mfma_f32_16x16x32_bf16 v[6:9], v[202:205], v[194:197], v[6:9]
	v_mfma_f32_16x16x32_bf16 v[2:5], v[210:213], v[194:197], v[2:5]
	v_mfma_f32_16x16x32_bf16 v[54:57], v[206:209], v[168:171], v[54:57]
	v_mfma_f32_16x16x32_bf16 v[50:53], v[214:217], v[168:171], v[50:53]
	v_mfma_f32_16x16x32_bf16 v[38:41], v[206:209], v[176:179], v[38:41]
	v_mfma_f32_16x16x32_bf16 v[34:37], v[214:217], v[176:179], v[34:37]
	v_mfma_f32_16x16x32_bf16 v[22:25], v[206:209], v[184:187], v[22:25]
	v_mfma_f32_16x16x32_bf16 v[18:21], v[214:217], v[184:187], v[18:21]
	v_mfma_f32_16x16x32_bf16 v[6:9], v[206:209], v[198:201], v[6:9]
	v_mfma_f32_16x16x32_bf16 v[2:5], v[214:217], v[198:201], v[2:5]
	s_setprio 0
	s_barrier
	ds_read_b128 v[130:133], v146
	ds_read_b128 v[134:137], v147
	ds_read_b128 v[156:159], v148
	ds_read_b128 v[160:163], v149
	ds_read_b128 v[164:167], v154 offset:32768
	ds_read_b128 v[168:171], v154 offset:33792
	ds_read_b128 v[172:175], v154 offset:34816
	ds_read_b128 v[176:179], v154 offset:35840
	ds_read_b128 v[180:183], v154 offset:36864
	ds_read_b128 v[184:187], v154 offset:37888
	ds_read_b128 v[194:197], v154 offset:38912
	ds_read_b128 v[198:201], v154 offset:39936
	s_add_u32 s58, s26, 0x80000
	s_addc_u32 s59, s27, 0
	s_mov_b32 s60, m0
	s_mov_b32 m0, s43
	s_nop 0
	global_load_lds_dwordx4 v1, s[58:59]
	s_mov_b32 m0, s60
	s_add_u32 s58, s26, 0xc0000
	s_addc_u32 s59, s27, 0
	s_mov_b32 s60, m0
	s_mov_b32 m0, s44
	s_nop 0
	global_load_lds_dwordx4 v1, s[58:59]
	s_mov_b32 m0, s60
	s_waitcnt lgkmcnt(8)
	s_barrier
	s_waitcnt lgkmcnt(0)
	s_setprio 1
	v_mfma_f32_16x16x32_bf16 v[126:129], v[130:133], v[164:167], v[126:129]
	v_mfma_f32_16x16x32_bf16 v[122:125], v[156:159], v[164:167], v[122:125]
	v_mfma_f32_16x16x32_bf16 v[110:113], v[130:133], v[172:175], v[110:113]
	v_mfma_f32_16x16x32_bf16 v[106:109], v[156:159], v[172:175], v[106:109]
	v_mfma_f32_16x16x32_bf16 v[94:97], v[130:133], v[180:183], v[94:97]
	v_mfma_f32_16x16x32_bf16 v[90:93], v[156:159], v[180:183], v[90:93]
	v_mfma_f32_16x16x32_bf16 v[78:81], v[130:133], v[194:197], v[78:81]
	v_mfma_f32_16x16x32_bf16 v[74:77], v[156:159], v[194:197], v[74:77]
	v_mfma_f32_16x16x32_bf16 v[126:129], v[134:137], v[168:171], v[126:129]
	v_mfma_f32_16x16x32_bf16 v[122:125], v[160:163], v[168:171], v[122:125]
	v_mfma_f32_16x16x32_bf16 v[110:113], v[134:137], v[176:179], v[110:113]
	v_mfma_f32_16x16x32_bf16 v[106:109], v[160:163], v[176:179], v[106:109]
	v_mfma_f32_16x16x32_bf16 v[94:97], v[134:137], v[184:187], v[94:97]
	v_mfma_f32_16x16x32_bf16 v[90:93], v[160:163], v[184:187], v[90:93]
	v_mfma_f32_16x16x32_bf16 v[78:81], v[134:137], v[198:201], v[78:81]
	v_mfma_f32_16x16x32_bf16 v[74:77], v[160:163], v[198:201], v[74:77]
	s_setprio 0
	s_barrier
	ds_read_b128 v[202:205], v150
	ds_read_b128 v[206:209], v151
	ds_read_b128 v[210:213], v152
	ds_read_b128 v[214:217], v153
	s_add_u32 s58, s24, 0x80
	s_addc_u32 s59, s25, 0
	s_mov_b32 s60, m0
	s_mov_b32 m0, s47
	s_nop 0
	global_load_lds_dwordx4 v1, s[58:59]
	s_mov_b32 m0, s60
	s_add_u32 s58, s24, 0x40080
	s_addc_u32 s59, s25, 0
	s_mov_b32 s60, m0
	s_mov_b32 m0, s48
	s_nop 0
	global_load_lds_dwordx4 v1, s[58:59]
	s_mov_b32 m0, s60
	s_barrier
	s_waitcnt lgkmcnt(0)
	s_setprio 1
	v_mfma_f32_16x16x32_bf16 v[118:121], v[202:205], v[164:167], v[118:121]
	v_mfma_f32_16x16x32_bf16 v[114:117], v[210:213], v[164:167], v[114:117]
	v_mfma_f32_16x16x32_bf16 v[102:105], v[202:205], v[172:175], v[102:105]
	v_mfma_f32_16x16x32_bf16 v[98:101], v[210:213], v[172:175], v[98:101]
	v_mfma_f32_16x16x32_bf16 v[86:89], v[202:205], v[180:183], v[86:89]
	v_mfma_f32_16x16x32_bf16 v[82:85], v[210:213], v[180:183], v[82:85]
	v_mfma_f32_16x16x32_bf16 v[70:73], v[202:205], v[194:197], v[70:73]
	v_mfma_f32_16x16x32_bf16 v[66:69], v[210:213], v[194:197], v[66:69]
	v_mfma_f32_16x16x32_bf16 v[118:121], v[206:209], v[168:171], v[118:121]
	v_mfma_f32_16x16x32_bf16 v[114:117], v[214:217], v[168:171], v[114:117]
	v_mfma_f32_16x16x32_bf16 v[102:105], v[206:209], v[176:179], v[102:105]
	v_mfma_f32_16x16x32_bf16 v[98:101], v[214:217], v[176:179], v[98:101]
	v_mfma_f32_16x16x32_bf16 v[86:89], v[206:209], v[184:187], v[86:89]
	v_mfma_f32_16x16x32_bf16 v[82:85], v[214:217], v[184:187], v[82:85]
	v_mfma_f32_16x16x32_bf16 v[70:73], v[206:209], v[198:201], v[70:73]
	v_mfma_f32_16x16x32_bf16 v[66:69], v[214:217], v[198:201], v[66:69]
	s_setprio 0
	s_barrier
	ds_read_b128 v[164:167], v154 offset:49152
	ds_read_b128 v[168:171], v154 offset:50176
	ds_read_b128 v[172:175], v154 offset:51200
	ds_read_b128 v[176:179], v154 offset:52224
	ds_read_b128 v[180:183], v154 offset:53248
	ds_read_b128 v[184:187], v154 offset:54272
	ds_read_b128 v[194:197], v154 offset:55296
	ds_read_b128 v[198:201], v154 offset:56320
	s_mov_b32 s58, m0
	s_mov_b32 m0, s49
	s_nop 0
	global_load_lds_dwordx4 v1, s[28:29]
	s_mov_b32 m0, s58
	s_add_u32 s26, s26, 0x40080
	s_addc_u32 s27, s27, 0
	s_mov_b32 s28, m0
	s_mov_b32 m0, s50
	s_nop 0
	global_load_lds_dwordx4 v1, s[26:27]
	s_mov_b32 m0, s28
	s_barrier
; #define PG8_STAGE(bufoff, gbase, voff) do { _Pragma("unroll") for (int _i = 0; _i < 2; ++_i) glds16_s((const void*)((const char*)(gbase) + _i * r64), (voff), ldsb + (unsigned)(bufoff) + ldsw + _i * 8192u); } while (0)
; #define PG8_WAIT_V(n) asm volatile("s_waitcnt vmcnt(" #n ")" ::: "memory")
; #define PG8_WAIT_L(n) asm volatile("s_waitcnt lgkmcnt(" #n ")" ::: "memory")
; #define PG8_BAR __builtin_amdgcn_s_barrier()
; #define PG8_SCHED __builtin_amdgcn_sched_barrier(0)
; #define PG8_HI do { if constexpr (FP8) asm volatile("s_setprio 1"); } while (0)
; #define PG8_LO do { if constexpr (FP8) asm volatile("s_setprio 0"); } while (0)
;     __device__ __forceinline__ void operator()(const f32x4 (&acc)[2][2][4][2], const Unit& u, int wr, int wc, int fr, int fq) const {
;         const int row0 = u.pm * BM + wr * 64 + fr, col0 = u.pn * BM + wc * 32 + 4 * fq;
;         f32x4 cs[2][2];
; #pragma unroll
;         for (int bj = 0; bj < 2; ++bj)
; #pragma unroll
;             for (int n = 0; n < 2; ++n) cs[bj][n] = (cscale ? *(const f32x4*)(cscale + col0 + bj * HALF + n * 16) : (f32x4){1.f, 1.f, 1.f, 1.f}) * ascale;
; #pragma unroll
;         for (int ai = 0; ai < 2; ++ai)
; #pragma unroll
;             for (int m = 0; m < 4; ++m) { const size_t off = (size_t)(row0 + ai * HALF + m * 16) * ldc + col0;
; #pragma unroll
;                 for (int bj = 0; bj < 2; ++bj)
; #pragma unroll
;                     for (int n = 0; n < 2; ++n) { f32x4 v = acc[ai][bj][m][n] * cs[bj][n];
;                         if (res) v += *(const f32x4*)(res + off + bj * HALF + n * 16);
;                         *(f32x4*)(out + off + bj * HALF + n * 16) = v; }
;                 asm volatile("" ::: "memory"); }
; template <class Epi, class Sched, bool FP8 = false>
; __device__ __forceinline__ void gemm_phase(LAS unsigned char* lds, const int Kb, const int nt  , const Sched& S, const Epi& E) {
;     ...
;             PG8_BAR; PG8_HI; PG8_WAIT_L(0); PG8_MMA(1, 0, B0, B08); PG8_BAR; PG8_LO; PG8_SCHED;
;             PG8_STAGE(PG8_SB(1, 1), b3 + hstep, voffB);
;             PG8_WAIT_V(6); PG8_BAR; PG8_HI; PG8_MMA(1, 1, B1, B18); PG8_BAR; PG8_LO;
;         }
;         { int l_; asm volatile("v_mbcnt_lo_u32_b32 %0, -1, 0\n\tv_mbcnt_hi_u32_b32 %0, -1, %0" : "=v"(l_));
;           E(acc, cur, wr, wc, l_ & 15, l_ >> 4); }
	s_waitcnt lgkmcnt(0)
	s_setprio 1
	v_mfma_f32_16x16x32_bf16 v[62:65], v[130:133], v[164:167], v[62:65]
	v_mfma_f32_16x16x32_bf16 v[58:61], v[156:159], v[164:167], v[58:61]
	v_mfma_f32_16x16x32_bf16 v[46:49], v[130:133], v[172:175], v[46:49]
	v_mfma_f32_16x16x32_bf16 v[42:45], v[156:159], v[172:175], v[42:45]
	v_mfma_f32_16x16x32_bf16 v[30:33], v[130:133], v[180:183], v[30:33]
	v_mfma_f32_16x16x32_bf16 v[26:29], v[156:159], v[180:183], v[26:29]
	v_mfma_f32_16x16x32_bf16 v[14:17], v[130:133], v[194:197], v[14:17]
	v_mfma_f32_16x16x32_bf16 v[10:13], v[156:159], v[194:197], v[10:13]
	v_mfma_f32_16x16x32_bf16 v[62:65], v[134:137], v[168:171], v[62:65]
	v_mfma_f32_16x16x32_bf16 v[58:61], v[160:163], v[168:171], v[58:61]
	v_mfma_f32_16x16x32_bf16 v[46:49], v[134:137], v[176:179], v[46:49]
	v_mfma_f32_16x16x32_bf16 v[42:45], v[160:163], v[176:179], v[42:45]
	v_mfma_f32_16x16x32_bf16 v[30:33], v[134:137], v[184:187], v[30:33]
	v_mfma_f32_16x16x32_bf16 v[26:29], v[160:163], v[184:187], v[26:29]
	v_mfma_f32_16x16x32_bf16 v[14:17], v[134:137], v[198:201], v[14:17]
	v_mfma_f32_16x16x32_bf16 v[10:13], v[160:163], v[198:201], v[10:13]
	s_setprio 0
	s_barrier
	s_add_u32 s26, s24, 0x80080
	s_addc_u32 s27, s25, 0
	s_mov_b32 s28, m0
	s_mov_b32 m0, s51
	s_nop 0
	global_load_lds_dwordx4 v1, s[26:27]
	s_mov_b32 m0, s28
	s_add_u32 s24, s24, 0xc0080
	s_addc_u32 s25, s25, 0
	s_mov_b32 s26, m0
	s_mov_b32 m0, s52
	s_nop 0
	global_load_lds_dwordx4 v1, s[24:25]
	s_mov_b32 m0, s26
	s_waitcnt vmcnt(6)
	s_barrier
	s_setprio 1
	v_mfma_f32_16x16x32_bf16 v[54:57], v[202:205], v[164:167], v[54:57]
	v_mfma_f32_16x16x32_bf16 v[50:53], v[210:213], v[164:167], v[50:53]
	v_mfma_f32_16x16x32_bf16 v[38:41], v[202:205], v[172:175], v[38:41]
	v_mfma_f32_16x16x32_bf16 v[34:37], v[210:213], v[172:175], v[34:37]
	v_mfma_f32_16x16x32_bf16 v[22:25], v[202:205], v[180:183], v[22:25]
	v_mfma_f32_16x16x32_bf16 v[18:21], v[210:213], v[180:183], v[18:21]
	v_mfma_f32_16x16x32_bf16 v[6:9], v[202:205], v[194:197], v[6:9]
	v_mfma_f32_16x16x32_bf16 v[2:5], v[210:213], v[194:197], v[2:5]
	v_mfma_f32_16x16x32_bf16 v[54:57], v[206:209], v[168:171], v[54:57]
	v_mfma_f32_16x16x32_bf16 v[50:53], v[214:217], v[168:171], v[50:53]
	v_mfma_f32_16x16x32_bf16 v[38:41], v[206:209], v[176:179], v[38:41]
	v_mfma_f32_16x16x32_bf16 v[34:37], v[214:217], v[176:179], v[34:37]
	v_mfma_f32_16x16x32_bf16 v[22:25], v[206:209], v[184:187], v[22:25]
	v_mfma_f32_16x16x32_bf16 v[18:21], v[214:217], v[184:187], v[18:21]
	v_mfma_f32_16x16x32_bf16 v[6:9], v[206:209], v[198:201], v[6:9]
	v_mfma_f32_16x16x32_bf16 v[2:5], v[214:217], v[198:201], v[2:5]
	s_setprio 0
	s_add_i32 s57, s57, 2
	s_add_u32 s22, s22, 0x100
	s_addc_u32 s23, s23, 0
	s_add_u32 s3, s3, 0x100
	s_addc_u32 s17, s17, 0
	s_cmp_gt_u32 s57, 29
	s_barrier
	s_cbranch_scc0 .LBB0_1715
	s_lshl_b32 s2, s2, 8
	v_mbcnt_lo_u32_b32 v132, -1, 0
	v_mbcnt_hi_u32_b32 v132, -1, v132
	s_add_i32 s2, s2, s45
	s_lshl_b32 s3, s56, 8
	v_ashrrev_i32_e32 v130, 2, v132
	s_or_b32 s3, s3, s46
	v_and_b32_e32 v130, -4, v130
	v_and_or_b32 v132, v132, 15, s2
	v_add_u32_e32 v130, s3, v130
	v_ashrrev_i32_e32 v133, 31, v132
	v_ashrrev_i32_e32 v131, 31, v130
	v_lshlrev_b64 v[134:135], 11, v[132:133]
	v_lshl_add_u64 v[136:137], v[134:135], 0, v[130:131]
	v_cndmask_b32_e64 v134, 0, 1, s[6:7]
	v_cmp_ne_u32_e64 s[2:3], 1, v134
	s_andn2_b64 vcc, exec, s[6:7]
	v_lshl_add_u64 v[134:135], v[136:137], 2, s[76:77]
	s_cbranch_vccnz .LBB0_1718
	s_waitcnt lgkmcnt(0)
	v_or_b32_e32 v250, 16, v132
	v_ashrrev_i32_e32 v251, 31, v250
	v_lshlrev_b64 v[250:251], 11, v[250:251]
	v_lshl_add_u64 v[250:251], v[250:251], 0, v[130:131]
	v_or_b32_e32 v252, 32, v132
	v_ashrrev_i32_e32 v253, 31, v252
	v_lshlrev_b64 v[252:253], 11, v[252:253]
	v_lshl_add_u64 v[252:253], v[252:253], 0, v[130:131]
	v_or_b32_e32 v254, 48, v132
	v_ashrrev_i32_e32 v255, 31, v254
	v_lshlrev_b64 v[254:255], 11, v[254:255]
	v_lshl_add_u64 v[254:255], v[254:255], 0, v[130:131]
	v_lshl_add_u64 v[134:135], v[136:137], 2, s[76:77]
	global_load_dwordx4 v[156:159], v[134:135], off
	global_load_dwordx4 v[160:163], v[134:135], off offset:64
	global_load_dwordx4 v[164:167], v[134:135], off offset:512
	global_load_dwordx4 v[168:171], v[134:135], off offset:576
	v_lshl_add_u64 v[134:135], v[250:251], 2, s[76:77]
	global_load_dwordx4 v[172:175], v[134:135], off
	global_load_dwordx4 v[176:179], v[134:135], off offset:64
	global_load_dwordx4 v[180:183], v[134:135], off offset:512
	global_load_dwordx4 v[184:187], v[134:135], off offset:576
	v_lshl_add_u64 v[134:135], v[252:253], 2, s[76:77]
	global_load_dwordx4 v[194:197], v[134:135], off
	global_load_dwordx4 v[198:201], v[134:135], off offset:64
	global_load_dwordx4 v[202:205], v[134:135], off offset:512
	global_load_dwordx4 v[206:209], v[134:135], off offset:576
	v_lshl_add_u64 v[134:135], v[254:255], 2, s[76:77]
	global_load_dwordx4 v[210:213], v[134:135], off
	global_load_dwordx4 v[214:217], v[134:135], off offset:64
	global_load_dwordx4 v[242:245], v[134:135], off offset:512
	global_load_dwordx4 v[246:249], v[134:135], off offset:576
	s_waitcnt vmcnt(0)
;     __device__ __forceinline__ void operator()(const f32x4 (&acc)[2][2][4][2], const Unit& u, int wr, int wc, int fr, int fq) const {
;     ...
;         for (int ai = 0; ai < 2; ++ai)
; #pragma unroll
;             for (int m = 0; m < 4; ++m) { const size_t off = (size_t)(row0 + ai * HALF + m * 16) * ldc + col0;
; #pragma unroll
;                 for (int bj = 0; bj < 2; ++bj)
; #pragma unroll
;                     for (int n = 0; n < 2; ++n) { f32x4 v = acc[ai][bj][m][n] * cs[bj][n];
;                         if (res) v += *(const f32x4*)(res + off + bj * HALF + n * 16);
;                         *(f32x4*)(out + off + bj * HALF + n * 16) = v; }
;                 asm volatile("" ::: "memory"); }
;     }
	v_pk_add_f32 v[126:127], v[126:127], v[156:157]
	v_pk_add_f32 v[128:129], v[128:129], v[158:159]
	v_pk_add_f32 v[122:123], v[122:123], v[160:161]
	v_pk_add_f32 v[124:125], v[124:125], v[162:163]
	v_pk_add_f32 v[118:119], v[118:119], v[164:165]
	v_pk_add_f32 v[120:121], v[120:121], v[166:167]
	v_pk_add_f32 v[114:115], v[114:115], v[168:169]
	v_pk_add_f32 v[116:117], v[116:117], v[170:171]
	v_lshl_add_u64 v[156:157], v[136:137], 2, s[4:5]
	global_store_dwordx4 v[156:157], v[126:129], off
	global_store_dwordx4 v[156:157], v[122:125], off offset:64
	global_store_dwordx4 v[156:157], v[118:121], off offset:512
	global_store_dwordx4 v[156:157], v[114:117], off offset:576
	v_pk_add_f32 v[110:111], v[110:111], v[172:173]
	v_pk_add_f32 v[112:113], v[112:113], v[174:175]
	v_pk_add_f32 v[106:107], v[106:107], v[176:177]
	v_pk_add_f32 v[108:109], v[108:109], v[178:179]
	v_pk_add_f32 v[102:103], v[102:103], v[180:181]
	v_pk_add_f32 v[104:105], v[104:105], v[182:183]
	v_pk_add_f32 v[98:99], v[98:99], v[184:185]
	v_pk_add_f32 v[100:101], v[100:101], v[186:187]
	v_lshl_add_u64 v[172:173], v[250:251], 2, s[4:5]
	global_store_dwordx4 v[172:173], v[110:113], off
	global_store_dwordx4 v[172:173], v[106:109], off offset:64
	global_store_dwordx4 v[172:173], v[102:105], off offset:512
	global_store_dwordx4 v[172:173], v[98:101], off offset:576
	v_pk_add_f32 v[94:95], v[94:95], v[194:195]
	v_pk_add_f32 v[96:97], v[96:97], v[196:197]
	v_pk_add_f32 v[90:91], v[90:91], v[198:199]
	v_pk_add_f32 v[92:93], v[92:93], v[200:201]
	v_pk_add_f32 v[86:87], v[86:87], v[202:203]
	v_pk_add_f32 v[88:89], v[88:89], v[204:205]
	v_pk_add_f32 v[82:83], v[82:83], v[206:207]
	v_pk_add_f32 v[84:85], v[84:85], v[208:209]
	v_lshl_add_u64 v[194:195], v[252:253], 2, s[4:5]
	global_store_dwordx4 v[194:195], v[94:97], off
	global_store_dwordx4 v[194:195], v[90:93], off offset:64
	global_store_dwordx4 v[194:195], v[86:89], off offset:512
	global_store_dwordx4 v[194:195], v[82:85], off offset:576
	v_pk_add_f32 v[78:79], v[78:79], v[210:211]
	v_pk_add_f32 v[80:81], v[80:81], v[212:213]
	v_pk_add_f32 v[74:75], v[74:75], v[214:215]
	v_pk_add_f32 v[76:77], v[76:77], v[216:217]
	v_pk_add_f32 v[70:71], v[70:71], v[242:243]
	v_pk_add_f32 v[72:73], v[72:73], v[244:245]
	v_pk_add_f32 v[66:67], v[66:67], v[246:247]
	v_pk_add_f32 v[68:69], v[68:69], v[248:249]
	v_lshl_add_u64 v[210:211], v[254:255], 2, s[4:5]
	global_store_dwordx4 v[210:211], v[78:81], off
	global_store_dwordx4 v[210:211], v[74:77], off offset:64
	global_store_dwordx4 v[210:211], v[70:73], off offset:512
	global_store_dwordx4 v[210:211], v[66:69], off offset:576
	s_mov_b64 s[22:23], 0x40000
	v_lshl_add_u64 v[136:137], v[136:137], 0, s[22:23]
	v_lshl_add_u64 v[250:251], v[250:251], 0, s[22:23]
	v_lshl_add_u64 v[252:253], v[252:253], 0, s[22:23]
	v_lshl_add_u64 v[254:255], v[254:255], 0, s[22:23]
	v_lshl_add_u64 v[134:135], v[136:137], 2, s[76:77]
	global_load_dwordx4 v[156:159], v[134:135], off
	global_load_dwordx4 v[160:163], v[134:135], off offset:64
	global_load_dwordx4 v[164:167], v[134:135], off offset:512
	global_load_dwordx4 v[168:171], v[134:135], off offset:576
	v_lshl_add_u64 v[134:135], v[250:251], 2, s[76:77]
	global_load_dwordx4 v[172:175], v[134:135], off
	global_load_dwordx4 v[176:179], v[134:135], off offset:64
	global_load_dwordx4 v[180:183], v[134:135], off offset:512
	global_load_dwordx4 v[184:187], v[134:135], off offset:576
	v_lshl_add_u64 v[134:135], v[252:253], 2, s[76:77]
	global_load_dwordx4 v[194:197], v[134:135], off
	global_load_dwordx4 v[198:201], v[134:135], off offset:64
	global_load_dwordx4 v[202:205], v[134:135], off offset:512
	global_load_dwordx4 v[206:209], v[134:135], off offset:576
	v_lshl_add_u64 v[134:135], v[254:255], 2, s[76:77]
	global_load_dwordx4 v[210:213], v[134:135], off
	global_load_dwordx4 v[214:217], v[134:135], off offset:64
	global_load_dwordx4 v[242:245], v[134:135], off offset:512
	global_load_dwordx4 v[246:249], v[134:135], off offset:576
	s_waitcnt vmcnt(0)
	v_pk_add_f32 v[62:63], v[62:63], v[156:157]
	v_pk_add_f32 v[64:65], v[64:65], v[158:159]
	v_pk_add_f32 v[58:59], v[58:59], v[160:161]
	v_pk_add_f32 v[60:61], v[60:61], v[162:163]
	v_pk_add_f32 v[54:55], v[54:55], v[164:165]
	v_pk_add_f32 v[56:57], v[56:57], v[166:167]
	v_pk_add_f32 v[50:51], v[50:51], v[168:169]
	v_pk_add_f32 v[52:53], v[52:53], v[170:171]
	v_lshl_add_u64 v[156:157], v[136:137], 2, s[4:5]
	global_store_dwordx4 v[156:157], v[62:65], off
	global_store_dwordx4 v[156:157], v[58:61], off offset:64
	global_store_dwordx4 v[156:157], v[54:57], off offset:512
	global_store_dwordx4 v[156:157], v[50:53], off offset:576
	v_pk_add_f32 v[46:47], v[46:47], v[172:173]
	v_pk_add_f32 v[48:49], v[48:49], v[174:175]
	v_pk_add_f32 v[42:43], v[42:43], v[176:177]
	v_pk_add_f32 v[44:45], v[44:45], v[178:179]
	v_pk_add_f32 v[38:39], v[38:39], v[180:181]
	v_pk_add_f32 v[40:41], v[40:41], v[182:183]
	v_pk_add_f32 v[34:35], v[34:35], v[184:185]
	v_pk_add_f32 v[36:37], v[36:37], v[186:187]
	v_lshl_add_u64 v[172:173], v[250:251], 2, s[4:5]
	global_store_dwordx4 v[172:173], v[46:49], off
	global_store_dwordx4 v[172:173], v[42:45], off offset:64
	global_store_dwordx4 v[172:173], v[38:41], off offset:512
	global_store_dwordx4 v[172:173], v[34:37], off offset:576
	v_pk_add_f32 v[30:31], v[30:31], v[194:195]
	v_pk_add_f32 v[32:33], v[32:33], v[196:197]
	v_pk_add_f32 v[26:27], v[26:27], v[198:199]
	v_pk_add_f32 v[28:29], v[28:29], v[200:201]
	v_pk_add_f32 v[22:23], v[22:23], v[202:203]
	v_pk_add_f32 v[24:25], v[24:25], v[204:205]
	v_pk_add_f32 v[18:19], v[18:19], v[206:207]
	v_pk_add_f32 v[20:21], v[20:21], v[208:209]
	v_lshl_add_u64 v[194:195], v[252:253], 2, s[4:5]
	global_store_dwordx4 v[194:195], v[30:33], off
	global_store_dwordx4 v[194:195], v[26:29], off offset:64
	global_store_dwordx4 v[194:195], v[22:25], off offset:512
	global_store_dwordx4 v[194:195], v[18:21], off offset:576
	v_pk_add_f32 v[14:15], v[14:15], v[210:211]
	v_pk_add_f32 v[16:17], v[16:17], v[212:213]
	v_pk_add_f32 v[10:11], v[10:11], v[214:215]
	v_pk_add_f32 v[12:13], v[12:13], v[216:217]
	v_pk_add_f32 v[6:7], v[6:7], v[242:243]
	v_pk_add_f32 v[8:9], v[8:9], v[244:245]
	v_pk_add_f32 v[2:3], v[2:3], v[246:247]
	v_pk_add_f32 v[4:5], v[4:5], v[248:249]
	v_lshl_add_u64 v[210:211], v[254:255], 2, s[4:5]
	global_store_dwordx4 v[210:211], v[14:17], off
	global_store_dwordx4 v[210:211], v[10:13], off offset:64
	global_store_dwordx4 v[210:211], v[6:9], off offset:512
	global_store_dwordx4 v[210:211], v[2:5], off offset:576
	s_branch .Lepi_done_1715
	global_load_dwordx4 v[156:159], v[134:135], off
	s_waitcnt vmcnt(0)
	v_pk_add_f32 v[128:129], v[128:129], v[158:159]
	v_pk_add_f32 v[126:127], v[126:127], v[156:157]

; __global__ void __launch_bounds__(NTHREADS, 2) mega_fwd(Args args) {
	.amdhsa_kernel _Z8mega_fwd4Args
		.amdhsa_group_segment_fixed_size 0
		.amdhsa_private_segment_fixed_size 0
		.amdhsa_kernarg_size 448
		.amdhsa_user_sgpr_count 2
		.amdhsa_user_sgpr_dispatch_ptr 0
		.amdhsa_user_sgpr_queue_ptr 0
		.amdhsa_user_sgpr_kernarg_segment_ptr 1
		.amdhsa_user_sgpr_dispatch_id 0
		.amdhsa_user_sgpr_kernarg_preload_length 0
		.amdhsa_user_sgpr_kernarg_preload_offset 0
		.amdhsa_user_sgpr_private_segment_size 0
		.amdhsa_uses_dynamic_stack 0
		.amdhsa_enable_private_segment 0
		.amdhsa_system_sgpr_workgroup_id_x 1
		.amdhsa_system_sgpr_workgroup_id_y 0
		.amdhsa_system_sgpr_workgroup_id_z 0
		.amdhsa_system_sgpr_workgroup_info 0
		.amdhsa_system_vgpr_workitem_id 0
		.amdhsa_next_free_vgpr 256
		.amdhsa_next_free_sgpr 100
		.amdhsa_accum_offset 256
		.amdhsa_reserve_vcc 1
		.amdhsa_float_round_mode_32 0
		.amdhsa_float_round_mode_16_64 0
		.amdhsa_float_denorm_mode_32 3
		.amdhsa_float_denorm_mode_16_64 3
		.amdhsa_dx10_clamp 1
		.amdhsa_ieee_mode 1
		.amdhsa_fp16_overflow 0
		.amdhsa_tg_split 0
		.amdhsa_exception_fp_ieee_invalid_op 0
		.amdhsa_exception_fp_denorm_src 0
		.amdhsa_exception_fp_ieee_div_zero 0
		.amdhsa_exception_fp_ieee_overflow 0
		.amdhsa_exception_fp_ieee_underflow 0
		.amdhsa_exception_fp_ieee_inexact 0
		.amdhsa_exception_int_div_zero 0
	.end_amdhsa_kernel

; __global__ void __launch_bounds__(NTHREADS, 2) mega_fwd(Args args) {
amdhsa.kernels:
  - .agpr_count:     0
    .args:
      - .offset:         0
        .size:           192
        .value_kind:     by_value
      - .offset:         192
        .size:           4
        .value_kind:     hidden_block_count_x
      - .offset:         196
        .size:           4
        .value_kind:     hidden_block_count_y
      - .offset:         200
        .size:           4
        .value_kind:     hidden_block_count_z
      - .offset:         204
        .size:           2
        .value_kind:     hidden_group_size_x
      - .offset:         206
        .size:           2
        .value_kind:     hidden_group_size_y
      - .offset:         208
        .size:           2
        .value_kind:     hidden_group_size_z
      - .offset:         210
        .size:           2
        .value_kind:     hidden_remainder_x
      - .offset:         212
        .size:           2
        .value_kind:     hidden_remainder_y
      - .offset:         214
        .size:           2
        .value_kind:     hidden_remainder_z
      - .offset:         232
        .size:           8
        .value_kind:     hidden_global_offset_x
      - .offset:         240
        .size:           8
        .value_kind:     hidden_global_offset_y
      - .offset:         248
        .size:           8
        .value_kind:     hidden_global_offset_z
      - .offset:         256
        .size:           2
        .value_kind:     hidden_grid_dims
      - .offset:         312
        .size:           4
        .value_kind:     hidden_dynamic_lds_size
    .group_segment_fixed_size: 0
    .kernarg_segment_align: 8
    .kernarg_segment_size: 448
    .language:       OpenCL C
    .language_version:
      - 2
      - 0
    .max_flat_workgroup_size: 512
    .name:           _Z8mega_fwd4Args
    .private_segment_fixed_size: 0
    .sgpr_count:     106
    .sgpr_spill_count: 332
    .symbol:         _Z8mega_fwd4Args.kd
    .uniform_work_group_size: 1
    .uses_dynamic_stack: false
    .vgpr_count:     256
    .vgpr_spill_count: 0
    .wavefront_size: 64
